# wave_sum butterflies (router, combine, MLA finalize, P0 tail) via DPP adds + permlane16/32 swaps instead of ds_bpermute round trips; bit-identical sums
# speedup vs baseline: 1.0173x; 1.0040x over previous
.LBB0_129:
	s_mov_b32 s10, 0
	s_ashr_i32 s11, s10, 31
	s_lshl_b64 s[10:11], s[10:11], 3
	s_add_u32 s10, s94, s10
	s_addc_u32 s11, s95, s11
	s_load_dwordx2 s[10:11], s[10:11], 0x0
	s_mov_b32 s0, 1
	s_ashr_i32 s1, s0, 31
	s_lshl_b64 s[0:1], s[0:1], 3
	s_waitcnt lgkmcnt(0)
	v_lshl_add_u64 v[34:35], s[10:11], 0, v[4:5]
	global_load_dwordx4 v[18:21], v[34:35], off
	global_load_dwordx4 v[22:25], v[34:35], off offset:1024
	global_load_dwordx4 v[26:29], v[34:35], off offset:2048
	global_load_dwordx4 v[30:33], v[34:35], off offset:3072
	s_add_u32 s0, s94, s0
	s_addc_u32 s1, s95, s1
	v_cmp_lt_i32_e32 vcc, v10, v9
	s_load_dwordx2 s[10:11], s[0:1], 0x0
	v_mov_b32_e32 v40, 0
	v_cndmask_b32_e32 v34, v8, v10, vcc
	v_cmp_lt_i32_e32 vcc, v11, v9
	v_lshlrev_b32_e32 v41, 2, v34
	s_add_i32 s4, s4, s2
	v_cndmask_b32_e32 v35, v8, v11, vcc
	v_cmp_lt_i32_e32 vcc, v12, v9
	v_lshlrev_b32_e32 v42, 2, v35
	v_lshl_add_u64 v[4:5], v[4:5], 0, s[8:9]
	v_cndmask_b32_e32 v36, v8, v12, vcc
	v_cmp_lt_i32_e32 vcc, v13, v9
	v_lshlrev_b32_e32 v43, 2, v36
	s_cmpk_gt_i32 s4, 0x3fff
	v_cndmask_b32_e32 v37, v8, v13, vcc
	v_lshlrev_b32_e32 v44, 2, v37
	s_waitcnt lgkmcnt(0)
	global_load_dwordx4 v[34:37], v1, s[10:11]
	global_load_dwordx4 v[160:163], v1, s[10:11] offset:1024
	global_load_dwordx4 v[164:167], v1, s[10:11] offset:2048
	global_load_dwordx4 v[168:171], v1, s[10:11] offset:3072
	v_cmp_lt_i32_e32 vcc, v14, v9
	s_waitcnt vmcnt(7)
	v_mul_f32_e32 v45, v19, v19
	v_mul_f32_e32 v46, v21, v21
	s_waitcnt vmcnt(6)
	v_mul_f32_e32 v47, v23, v23
	v_mul_f32_e32 v48, v25, v25
	s_waitcnt vmcnt(5)
	v_mul_f32_e32 v49, v27, v27
	v_mul_f32_e32 v50, v29, v29
	v_fmac_f32_e32 v45, v18, v18
	v_fmac_f32_e32 v46, v20, v20
	v_fmac_f32_e32 v47, v22, v22
	v_fmac_f32_e32 v48, v24, v24
	s_waitcnt vmcnt(4)
	v_mul_f32_e32 v51, v31, v31
	v_mul_f32_e32 v52, v33, v33
	v_fmac_f32_e32 v49, v26, v26
	v_fmac_f32_e32 v50, v28, v28
	v_add_f32_e32 v45, v45, v46
	v_add_f32_e32 v46, v47, v48
	v_fmac_f32_e32 v51, v30, v30
	v_fmac_f32_e32 v52, v32, v32
	v_add_f32_e32 v47, v49, v50
	v_add_f32_e32 v45, v45, v46
	v_add_f32_e32 v48, v51, v52
	v_add_f32_e32 v45, v45, v47
	v_add_f32_e32 v45, v45, v48
	v_cndmask_b32_e32 v38, v8, v14, vcc
	v_lshlrev_b32_e32 v38, 2, v38
	v_cmp_lt_i32_e32 vcc, v15, v9
	s_waitcnt lgkmcnt(0)
	s_nop 1
	v_add_f32_dpp v41, v45, v45 quad_perm:[1,0,3,2] row_mask:0xf bank_mask:0xf
	v_cndmask_b32_e32 v39, v8, v15, vcc
	v_lshlrev_b32_e32 v39, 2, v39
	s_waitcnt lgkmcnt(0)
	s_nop 1
	v_add_f32_dpp v41, v41, v41 quad_perm:[2,3,0,1] row_mask:0xf bank_mask:0xf
	s_waitcnt lgkmcnt(0)
	s_nop 1
	v_add_f32_dpp v41, v41, v41 row_half_mirror row_mask:0xf bank_mask:0xf
	s_waitcnt lgkmcnt(0)
	s_nop 1
	v_add_f32_dpp v41, v41, v41 row_ror:8 row_mask:0xf bank_mask:0xf
	s_waitcnt lgkmcnt(0)
	v_mov_b32_e32 v38, v41
	s_nop 1
	v_permlane16_swap_b32_e32 v38, v41
	v_add_f32_e32 v38, v41, v38
	s_waitcnt lgkmcnt(0)
	v_mov_b32_e32 v39, v38
	s_nop 1
	v_permlane32_swap_b32_e32 v39, v38
	v_add_f32_e32 v38, v38, v39
	v_fmamk_f32 v38, v38, 0x3a800000, v16
	v_mul_f32_e32 v39, 0x4f800000, v38
	v_cmp_gt_f32_e32 vcc, s3, v38
	s_nop 1
	v_cndmask_b32_e32 v38, v38, v39, vcc
	v_sqrt_f32_e32 v39, v38
	s_nop 0
	v_add_u32_e32 v41, -1, v39
	v_add_u32_e32 v42, 1, v39
	v_fma_f32 v43, -v41, v39, v38
	v_fma_f32 v44, -v42, v39, v38
	v_cmp_ge_f32_e64 s[0:1], 0, v43
	s_nop 1
	v_cndmask_b32_e64 v39, v39, v41, s[0:1]
	v_cmp_lt_f32_e64 s[0:1], 0, v44
	s_nop 1
	v_cndmask_b32_e64 v39, v39, v42, s[0:1]
	v_mul_f32_e32 v41, 0x37800000, v39
	v_cndmask_b32_e32 v39, v39, v41, vcc
	v_cmp_class_f32_e32 vcc, v38, v17
	s_nop 1
	v_cndmask_b32_e32 v38, v39, v38, vcc
	v_div_scale_f32 v39, s[0:1], v38, v38, 1.0
	v_rcp_f32_e32 v42, v39
	v_div_scale_f32 v41, vcc, 1.0, v38, 1.0
	v_fma_f32 v43, -v39, v42, 1.0
	v_fmac_f32_e32 v42, v43, v42
	v_mul_f32_e32 v43, v41, v42
	v_fma_f32 v44, -v39, v43, v41
	v_fmac_f32_e32 v43, v44, v42
	v_fma_f32 v39, -v39, v43, v41
	v_div_fmas_f32 v39, v39, v42, v43
	v_div_fixup_f32 v38, v39, v38, 1.0
	v_mul_f32_e32 v18, v18, v38
	v_mul_f32_e32 v19, v19, v38
	s_waitcnt vmcnt(3)
	v_mul_f32_e32 v18, v34, v18
	v_mul_f32_e32 v19, v35, v19
	v_cvt_pk_fp8_f32 v40, v18, v19
	v_mul_f32_e32 v20, v20, v38
	v_mul_f32_e32 v21, v21, v38
	v_mul_f32_e32 v20, v36, v20
	v_mul_f32_e32 v21, v37, v21
	v_cvt_pk_fp8_f32 v40, v20, v21 op_sel:[0,0,1]
	v_mul_f32_e32 v22, v22, v38
	v_mul_f32_e32 v23, v23, v38
	v_mov_b32_e32 v34, 0
	global_store_dword v[2:3], v40, off offset:-512
	v_mul_f32_e32 v24, v24, v38
	v_mul_f32_e32 v25, v25, v38
	s_waitcnt vmcnt(3)
	v_mov_b32_e32 v18, v160
	v_mov_b32_e32 v19, v161
	v_mov_b32_e32 v20, v162
	v_mov_b32_e32 v21, v163
	v_mul_f32_e32 v18, v18, v22
	v_mul_f32_e32 v19, v19, v23
	v_cvt_pk_fp8_f32 v34, v18, v19
	v_mul_f32_e32 v20, v20, v24
	v_mul_f32_e32 v21, v21, v25
	v_mul_f32_e32 v23, v26, v38
	v_cvt_pk_fp8_f32 v34, v20, v21 op_sel:[0,0,1]
	v_mul_f32_e32 v24, v27, v38
	v_mov_b32_e32 v22, 0
	v_mul_f32_e32 v25, v28, v38
	global_store_dword v[2:3], v34, off offset:-256
	v_mul_f32_e32 v26, v29, v38
	s_waitcnt vmcnt(3)
	v_mov_b32_e32 v18, v164
	v_mov_b32_e32 v19, v165
	v_mov_b32_e32 v20, v166
	v_mov_b32_e32 v21, v167
	v_mul_f32_e32 v18, v23, v18
	v_mul_f32_e32 v19, v24, v19
	v_cvt_pk_fp8_f32 v22, v18, v19
	v_mul_f32_e32 v20, v25, v20
	v_mul_f32_e32 v18, v26, v21
	v_mul_f32_e32 v23, v30, v38
	v_cvt_pk_fp8_f32 v22, v20, v18 op_sel:[0,0,1]
	v_mul_f32_e32 v24, v31, v38
	v_mul_f32_e32 v25, v32, v38
	v_mul_f32_e32 v26, v33, v38
	global_store_dword v[2:3], v22, off
	v_mov_b32_e32 v22, 0
	s_waitcnt vmcnt(3)
	v_mov_b32_e32 v18, v168
	v_mov_b32_e32 v19, v169
	v_mov_b32_e32 v20, v170
	v_mov_b32_e32 v21, v171
	v_mul_f32_e32 v18, v23, v18
	v_mul_f32_e32 v19, v24, v19
	v_cvt_pk_fp8_f32 v22, v18, v19
	v_mul_f32_e32 v18, v25, v20
	v_mul_f32_e32 v19, v26, v21
	v_cvt_pk_fp8_f32 v22, v18, v19 op_sel:[0,0,1]
	global_store_dword v[2:3], v22, off offset:256
	v_lshl_add_u64 v[2:3], v[2:3], 0, s[6:7]
	s_cbranch_scc0 .LBB0_129

.LBB0_596:
	s_and_b32 s0, s4, 0x1fff
	v_cvt_f64_u32_e32 v[56:57], s0
	v_mul_f64 v[58:59], v[16:17], v[56:57]
	v_mul_f64 v[74:75], v[58:59], s[2:3]
	v_rndne_f64_e32 v[74:75], v[74:75]
	v_fma_f64 v[58:59], v[58:59], s[2:3], -v[74:75]
	v_cvt_f32_f64_e32 v1, v[58:59]
	v_mul_f64 v[58:59], v[60:61], v[56:57]
	v_mul_f64 v[74:75], v[58:59], s[2:3]
	v_rndne_f64_e32 v[74:75], v[74:75]
	v_fma_f64 v[58:59], v[58:59], s[2:3], -v[74:75]
	v_sin_f32_e32 v99, v1
	v_cos_f32_e32 v102, v1
	v_cvt_f32_f64_e32 v1, v[58:59]
	v_mul_f64 v[58:59], v[62:63], v[56:57]
	v_mul_f64 v[74:75], v[58:59], s[2:3]
	v_rndne_f64_e32 v[74:75], v[74:75]
	v_fma_f64 v[58:59], v[58:59], s[2:3], -v[74:75]
	v_mul_f64 v[56:57], v[64:65], v[56:57]
	v_sin_f32_e32 v97, v1
	v_cos_f32_e32 v101, v1
	v_cvt_f32_f64_e32 v1, v[58:59]
	v_mul_f64 v[58:59], v[56:57], s[2:3]
	v_rndne_f64_e32 v[58:59], v[58:59]
	v_fma_f64 v[56:57], v[56:57], s[2:3], -v[58:59]
	v_lshl_add_u64 v[76:77], v[72:73], 0, s[72:73]
	v_sin_f32_e32 v96, v1
	v_cos_f32_e32 v100, v1
	v_cvt_f32_f64_e32 v1, v[56:57]
	v_add_co_u32_e32 v56, vcc, s5, v76
	v_lshl_add_u64 v[74:75], v[70:71], 0, s[72:73]
	s_nop 0
	v_addc_co_u32_e32 v57, vcc, 0, v77, vcc
	global_load_dwordx4 v[104:107], v[56:57], off
	v_add_co_u32_e32 v56, vcc, s5, v74
	v_sin_f32_e32 v2, v1
	s_nop 0
	v_addc_co_u32_e32 v57, vcc, 0, v75, vcc
	v_cos_f32_e32 v98, v1
	global_load_dword v1, v[56:57], off offset:128
	global_load_dword v103, v[56:57], off offset:160
	v_lshl_add_u64 v[56:57], v[68:69], 0, s[72:73]
	global_load_dwordx4 v[56:59], v[56:57], off
	v_lshl_add_u64 v[78:79], v[66:67], 0, s[72:73]
	s_brev_b32 s0, 32
	v_add_co_u32_e32 v78, vcc, s0, v78
	s_add_i32 s4, s4, s6
	s_nop 0
	v_addc_co_u32_e32 v79, vcc, 0, v79, vcc
	global_load_dwordx2 v[80:81], v[78:79], off offset:1536
	s_nop 0
	global_load_dwordx2 v[78:79], v[78:79], off offset:1600
	v_lshl_add_u64 v[66:67], v[66:67], 0, s[8:9]
	v_lshl_add_u64 v[68:69], v[68:69], 0, s[8:9]
	v_lshl_add_u64 v[70:71], v[70:71], 0, s[10:11]
	v_lshl_add_u64 v[72:73], v[72:73], 0, s[10:11]
	s_cmpk_lt_i32 s4, 0x4000
	s_waitcnt vmcnt(5)
	v_cvt_pk_f32_fp8_e32 v[90:91], v106
	v_cvt_pk_f32_fp8_e32 v[82:83], v104
	v_cvt_pk_f32_fp8_sdwa v[92:93], v106 src0_sel:WORD_1
	v_cvt_pk_f32_fp8_sdwa v[84:85], v104 src0_sel:WORD_1
	v_cvt_pk_f32_fp8_e32 v[112:113], v107
	v_cvt_pk_f32_fp8_e32 v[86:87], v105
	v_cvt_pk_f32_fp8_sdwa v[114:115], v107 src0_sel:WORD_1
	v_pk_mul_f32 v[106:107], v[90:91], v[90:91]
	v_pk_mul_f32 v[110:111], v[92:93], v[92:93]
	v_pk_fma_f32 v[106:107], v[82:83], v[82:83], v[106:107]
	v_cvt_pk_f32_fp8_sdwa v[88:89], v105 src0_sel:WORD_1
	s_waitcnt vmcnt(4)
	v_cvt_pk_f32_fp8_e32 v[104:105], v1
	v_cvt_pk_f32_fp8_sdwa v[116:117], v1 src0_sel:WORD_1
	v_pk_fma_f32 v[110:111], v[84:85], v[84:85], v[110:111]
	v_add_f32_e32 v1, v106, v107
	s_waitcnt vmcnt(3)
	v_cvt_pk_f32_fp8_e32 v[108:109], v103
	v_pk_mul_f32 v[120:121], v[112:113], v[112:113]
	v_add_f32_e32 v1, v1, v110
	v_pk_fma_f32 v[120:121], v[86:87], v[86:87], v[120:121]
	v_add_f32_e32 v1, v111, v1
	v_cvt_pk_f32_fp8_sdwa v[118:119], v103 src0_sel:WORD_1
	v_pk_mul_f32 v[122:123], v[114:115], v[114:115]
	v_add_f32_e32 v1, v120, v1
	v_pk_fma_f32 v[122:123], v[88:89], v[88:89], v[122:123]
	v_add_f32_e32 v1, v121, v1
	v_pk_mul_f32 v[124:125], v[108:109], v[108:109]
	v_add_f32_e32 v1, v122, v1
	v_pk_fma_f32 v[124:125], v[104:105], v[104:105], v[124:125]
	v_add_f32_e32 v1, v123, v1
	v_pk_mul_f32 v[126:127], v[118:119], v[118:119]
	v_add_f32_e32 v1, v124, v1
	v_pk_fma_f32 v[126:127], v[116:117], v[116:117], v[126:127]
	v_add_f32_e32 v1, v125, v1
	v_add_f32_e32 v1, v126, v1
	v_add_f32_e32 v1, v127, v1
	s_waitcnt lgkmcnt(0)
	s_nop 1
	v_add_f32_dpp v1, v1, v1 quad_perm:[1,0,3,2] row_mask:0xf bank_mask:0xf
	s_waitcnt lgkmcnt(0)
	s_nop 1
	v_add_f32_dpp v1, v1, v1 quad_perm:[2,3,0,1] row_mask:0xf bank_mask:0xf
	s_waitcnt lgkmcnt(0)
	s_nop 1
	v_add_f32_dpp v1, v1, v1 row_half_mirror row_mask:0xf bank_mask:0xf
	v_fmamk_f32 v1, v1, 0x3baaaaab, v220
	v_cmp_gt_f32_e32 vcc, s93, v1
	v_mul_f32_e32 v103, 0x4f800000, v1
	s_nop 0
	v_cndmask_b32_e32 v1, v1, v103, vcc
	v_sqrt_f32_e32 v103, v1
	s_nop 0
	v_add_u32_e32 v106, -1, v103
	v_fma_f32 v107, -v106, v103, v1
	v_cmp_ge_f32_e64 s[0:1], 0, v107
	v_add_u32_e32 v107, 1, v103
	s_nop 0
	v_cndmask_b32_e64 v106, v103, v106, s[0:1]
	v_fma_f32 v103, -v107, v103, v1
	v_cmp_lt_f32_e64 s[0:1], 0, v103
	s_nop 1
	v_cndmask_b32_e64 v103, v106, v107, s[0:1]
	v_mul_f32_e32 v106, 0x37800000, v103
	v_cndmask_b32_e32 v103, v103, v106, vcc
	v_cmp_class_f32_e32 vcc, v1, v221
	s_nop 1
	v_cndmask_b32_e32 v1, v103, v1, vcc
	v_div_scale_f32 v103, s[0:1], v1, v1, s7
	v_rcp_f32_e32 v106, v103
	s_nop 0
	v_fma_f32 v107, -v103, v106, 1.0
	v_fmac_f32_e32 v106, v107, v106
	v_div_scale_f32 v107, vcc, s7, v1, s7
	v_mul_f32_e32 v110, v107, v106
	v_fma_f32 v111, -v103, v110, v107
	v_fmac_f32_e32 v110, v111, v106
	v_fma_f32 v103, -v103, v110, v107
	v_div_fmas_f32 v103, v103, v106, v110
	v_div_fixup_f32 v111, v103, v1, s7
	v_mul_f32_e32 v103, v108, v111
	v_mul_f32_e32 v1, v104, v111
	v_mul_f32_e32 v104, v44, v103
	v_mul_f32_e32 v1, v40, v1
	v_mul_f32_e32 v103, v99, v104
	v_fma_f32 v107, v102, v1, -v103
	v_mul_f32_e32 v103, v99, v1
	v_fmac_f32_e32 v103, v102, v104
	v_mul_f32_e32 v104, v109, v111
	v_mul_f32_e32 v1, v105, v111
	v_mul_f32_e32 v105, v45, v104
	v_mul_f32_e32 v1, v41, v1
	v_mul_f32_e32 v104, v97, v105
	v_fma_f32 v108, v101, v1, -v104
	v_mul_f32_e32 v104, v97, v1
	v_fmac_f32_e32 v104, v101, v105
	v_mul_f32_e32 v105, v118, v111
	v_mul_f32_e32 v1, v116, v111
	v_mul_f32_e32 v106, v46, v105
	v_mul_f32_e32 v1, v42, v1
	v_mul_f32_e32 v105, v96, v106
	v_fma_f32 v109, v100, v1, -v105
	v_mul_f32_e32 v105, v96, v1
	v_fmac_f32_e32 v105, v100, v106
	v_mul_f32_e32 v106, v119, v111
	v_mul_f32_e32 v1, v117, v111
	v_mul_f32_e32 v116, v47, v106
	v_mul_f32_e32 v1, v43, v1
	v_mul_f32_e32 v106, v2, v116
	v_mul_f32_e32 v112, v112, v111
	v_mul_f32_e32 v113, v113, v111
	v_fma_f32 v110, v98, v1, -v106
	v_mul_f32_e32 v106, v2, v1
	v_mul_f32_e32 v1, v114, v111
	v_mul_f32_e32 v114, v115, v111
	v_mul_f32_e32 v112, v20, v112
	v_mul_f32_e32 v113, v21, v113
	v_mov_b32_e32 v115, v3
	v_cvt_pk_fp8_f32 v115, v112, v113
	v_mul_f32_e32 v1, v22, v1
	v_mul_f32_e32 v114, v23, v114
	v_mul_f32_e32 v90, v90, v111
	v_mul_f32_e32 v91, v91, v111
	v_cvt_pk_fp8_f32 v115, v1, v114 op_sel:[0,0,1]
	v_mul_f32_e32 v90, v12, v90
	v_mul_f32_e32 v91, v13, v91
	v_mov_b32_e32 v114, v3
	v_cvt_pk_fp8_f32 v114, v90, v91
	v_mul_f32_e32 v86, v86, v111
	v_mul_f32_e32 v87, v87, v111
	v_mul_f32_e32 v86, v8, v86
	v_mul_f32_e32 v87, v9, v87
	v_mov_b32_e32 v113, v3
	v_mul_f32_e32 v1, v92, v111
	v_mul_f32_e32 v92, v93, v111
	v_cvt_pk_fp8_f32 v113, v86, v87
	v_mul_f32_e32 v82, v82, v111
	v_mul_f32_e32 v83, v83, v111
	v_mul_f32_e32 v1, v14, v1
	v_mul_f32_e32 v92, v15, v92
	v_mul_f32_e32 v82, v4, v82
	v_mul_f32_e32 v83, v5, v83
	v_mov_b32_e32 v112, v3
	v_cvt_pk_fp8_f32 v114, v1, v92 op_sel:[0,0,1]
	v_mul_f32_e32 v1, v88, v111
	v_mul_f32_e32 v88, v89, v111
	v_cvt_pk_fp8_f32 v112, v82, v83
	v_mul_f32_e32 v1, v10, v1
	v_mul_f32_e32 v88, v11, v88
	v_cvt_pk_fp8_f32 v113, v1, v88 op_sel:[0,0,1]
	v_mul_f32_e32 v1, v84, v111
	v_mul_f32_e32 v84, v85, v111
	v_mul_f32_e32 v1, v6, v1
	v_mul_f32_e32 v84, v7, v84
	v_cvt_pk_fp8_f32 v112, v1, v84 op_sel:[0,0,1]
	v_mov_b32_e32 v1, v3
	v_cvt_pk_fp8_f32 v1, v107, v108
	v_add_co_u32_e32 v82, vcc, s14, v76
	v_fmac_f32_e32 v106, v98, v116
	v_cvt_pk_fp8_f32 v1, v109, v110 op_sel:[0,0,1]
	v_addc_co_u32_e32 v83, vcc, 0, v77, vcc
	global_store_dwordx4 v[82:83], v[112:115], off
	v_add_co_u32_e32 v82, vcc, s14, v74
	s_waitcnt vmcnt(3)
	v_cvt_pk_f32_fp8_e32 v[88:89], v58
	v_addc_co_u32_e32 v83, vcc, 0, v75, vcc
	global_store_dword v[82:83], v1, off offset:128
	v_mov_b32_e32 v1, v3
	v_cvt_pk_fp8_f32 v1, v103, v104
	v_cvt_pk_f32_fp8_sdwa v[90:91], v58 src0_sel:WORD_1
	v_cvt_pk_f32_fp8_sdwa v[84:85], v56 src0_sel:WORD_1
	v_cvt_pk_f32_fp8_e32 v[86:87], v57
	v_cvt_pk_fp8_f32 v1, v105, v106 op_sel:[0,0,1]
	v_cvt_pk_f32_fp8_e32 v[104:105], v59
	v_cvt_pk_f32_fp8_sdwa v[106:107], v59 src0_sel:WORD_1
	v_pk_mul_f32 v[58:59], v[88:89], v[88:89]
	global_store_dword v[82:83], v1, off offset:160
	v_cvt_pk_f32_fp8_e32 v[82:83], v56
	v_pk_mul_f32 v[92:93], v[90:91], v[90:91]
	v_cvt_pk_f32_fp8_sdwa v[56:57], v57 src0_sel:WORD_1
	v_pk_fma_f32 v[92:93], v[84:85], v[84:85], v[92:93]
	v_pk_fma_f32 v[58:59], v[82:83], v[82:83], v[58:59]
	v_pk_mul_f32 v[108:109], v[104:105], v[104:105]
	v_add_f32_e32 v58, v58, v59
	v_add_f32_e32 v58, v58, v92
	v_pk_fma_f32 v[108:109], v[86:87], v[86:87], v[108:109]
	v_add_f32_e32 v58, v93, v58
	v_pk_mul_f32 v[110:111], v[106:107], v[106:107]
	v_add_f32_e32 v58, v108, v58
	s_waitcnt vmcnt(4)
	v_lshlrev_b32_e32 v1, 16, v80
	v_and_b32_e32 v112, 0xffff0000, v80
	s_waitcnt vmcnt(3)
	v_lshlrev_b32_e32 v80, 16, v78
	v_pk_fma_f32 v[110:111], v[56:57], v[56:57], v[110:111]
	v_add_f32_e32 v58, v109, v58
	v_add_f32_e32 v58, v110, v58
	v_mul_f32_e32 v59, v80, v80
	v_and_b32_e32 v78, 0xffff0000, v78
	v_add_f32_e32 v58, v111, v58
	v_fmac_f32_e32 v59, v1, v1
	v_add_f32_e32 v58, v59, v58
	v_mul_f32_e32 v59, v78, v78
	v_fmac_f32_e32 v59, v112, v112
	v_and_b32_e32 v110, 0xffff0000, v79
	v_lshlrev_b32_e32 v111, 16, v79
	v_add_f32_e32 v92, v59, v58
	v_and_b32_e32 v108, 0xffff0000, v81
	v_lshlrev_b32_e32 v109, 16, v81
	v_pk_mul_f32 v[58:59], v[110:111], v[110:111]
	s_nop 0
	v_pk_fma_f32 v[58:59], v[108:109], v[108:109], v[58:59]
	s_nop 0
	v_add_f32_e32 v59, v59, v92
	v_add_f32_e32 v58, v58, v59
	s_waitcnt lgkmcnt(0)
	s_nop 1
	v_add_f32_dpp v58, v58, v58 quad_perm:[1,0,3,2] row_mask:0xf bank_mask:0xf
	s_waitcnt lgkmcnt(0)
	s_nop 1
	v_add_f32_dpp v58, v58, v58 quad_perm:[2,3,0,1] row_mask:0xf bank_mask:0xf
	s_waitcnt lgkmcnt(0)
	s_nop 1
	v_add_f32_dpp v58, v58, v58 row_half_mirror row_mask:0xf bank_mask:0xf
	v_fmamk_f32 v58, v58, 0x3baaaaab, v220
	v_cmp_gt_f32_e32 vcc, s93, v58
	v_mul_f32_e32 v59, 0x4f800000, v58
	s_nop 0
	v_cndmask_b32_e32 v58, v58, v59, vcc
	v_sqrt_f32_e32 v59, v58
	s_nop 0
	v_add_u32_e32 v79, -1, v59
	v_fma_f32 v81, -v79, v59, v58
	v_cmp_ge_f32_e64 s[0:1], 0, v81
	v_add_u32_e32 v81, 1, v59
	s_nop 0
	v_cndmask_b32_e64 v79, v59, v79, s[0:1]
	v_fma_f32 v59, -v81, v59, v58
	v_cmp_lt_f32_e64 s[0:1], 0, v59
	s_nop 1
	v_cndmask_b32_e64 v59, v79, v81, s[0:1]
	v_mul_f32_e32 v79, 0x37800000, v59
	v_cndmask_b32_e32 v59, v59, v79, vcc
	v_cmp_class_f32_e32 vcc, v58, v221
	s_nop 1
	v_cndmask_b32_e32 v58, v59, v58, vcc
	v_div_scale_f32 v59, s[0:1], v58, v58, 1.0
	v_rcp_f32_e32 v79, v59
	s_mov_b32 s0, 0x15000000
	v_fma_f32 v81, -v59, v79, 1.0
	v_fmac_f32_e32 v79, v81, v79
	v_div_scale_f32 v81, vcc, 1.0, v58, 1.0
	v_mul_f32_e32 v92, v81, v79
	v_fma_f32 v93, -v59, v92, v81
	v_fmac_f32_e32 v92, v93, v79
	v_fma_f32 v59, -v59, v92, v81
	v_div_fmas_f32 v59, v59, v79, v92
	v_div_fixup_f32 v103, v59, v58, 1.0
	v_mul_f32_e32 v58, v103, v80
	v_mul_f32_e32 v1, v103, v1
	v_mul_f32_e32 v58, v52, v58
	v_mul_f32_e32 v1, v48, v1
	v_mul_f32_e32 v59, v99, v58
	v_fma_f32 v80, v102, v1, -v59
	v_mul_f32_e32 v58, v102, v58
	v_mul_f32_e32 v59, v103, v78
	v_fmac_f32_e32 v58, v99, v1
	v_mul_f32_e32 v1, v103, v112
	v_mul_f32_e32 v59, v53, v59
	v_mul_f32_e32 v1, v49, v1
	v_mul_f32_e32 v78, v97, v59
	v_fma_f32 v81, v101, v1, -v78
	v_mul_f32_e32 v59, v101, v59
	v_mul_f32_e32 v78, v103, v111
	v_fmac_f32_e32 v59, v97, v1
	v_mul_f32_e32 v1, v103, v109
	v_mul_f32_e32 v78, v54, v78
	v_mul_f32_e32 v1, v50, v1
	v_mul_f32_e32 v79, v96, v78
	v_mul_f32_e32 v78, v100, v78
	v_fma_f32 v92, v100, v1, -v79
	v_fmac_f32_e32 v78, v96, v1
	v_mul_f32_e32 v79, v103, v110
	v_mul_f32_e32 v96, v104, v103
	v_mul_f32_e32 v97, v105, v103
	v_mul_f32_e32 v1, v103, v108
	v_mul_f32_e32 v79, v55, v79
	v_mul_f32_e32 v96, v36, v96
	v_mul_f32_e32 v97, v37, v97
	v_mov_b32_e32 v99, v3
	v_mul_f32_e32 v1, v51, v1
	v_mul_f32_e32 v93, v2, v79
	v_cvt_pk_fp8_f32 v99, v96, v97
	v_mul_f32_e32 v88, v88, v103
	v_mul_f32_e32 v89, v89, v103
	v_fma_f32 v93, v98, v1, -v93
	v_mul_f32_e32 v79, v98, v79
	v_mul_f32_e32 v88, v32, v88
	v_mul_f32_e32 v89, v33, v89
	v_mov_b32_e32 v98, v3
	v_fmac_f32_e32 v79, v2, v1
	v_mul_f32_e32 v1, v106, v103
	v_mul_f32_e32 v2, v107, v103
	v_cvt_pk_fp8_f32 v98, v88, v89
	v_mul_f32_e32 v1, v38, v1
	v_mul_f32_e32 v2, v39, v2
	v_cvt_pk_fp8_f32 v99, v1, v2 op_sel:[0,0,1]
	v_mul_f32_e32 v1, v90, v103
	v_mul_f32_e32 v2, v91, v103
	v_mul_f32_e32 v1, v34, v1
	v_mul_f32_e32 v2, v35, v2
	v_cvt_pk_fp8_f32 v98, v1, v2 op_sel:[0,0,1]
	v_mul_f32_e32 v1, v56, v103
	v_mul_f32_e32 v2, v57, v103
	v_mul_f32_e32 v56, v86, v103
	v_mul_f32_e32 v57, v87, v103
	v_mul_f32_e32 v56, v28, v56
	v_mul_f32_e32 v57, v29, v57
	v_mov_b32_e32 v97, v3
	v_cvt_pk_fp8_f32 v97, v56, v57
	v_mul_f32_e32 v56, v82, v103
	v_mul_f32_e32 v57, v83, v103
	v_mul_f32_e32 v56, v24, v56
	v_mul_f32_e32 v57, v25, v57
	v_mov_b32_e32 v96, v3
	v_cvt_pk_fp8_f32 v96, v56, v57
	v_mul_f32_e32 v1, v30, v1
	v_mul_f32_e32 v2, v31, v2
	v_cvt_pk_fp8_f32 v97, v1, v2 op_sel:[0,0,1]
	v_mul_f32_e32 v1, v84, v103
	v_mul_f32_e32 v2, v85, v103
	v_mul_f32_e32 v1, v26, v1
	v_mul_f32_e32 v2, v27, v2
	v_cvt_pk_fp8_f32 v96, v1, v2 op_sel:[0,0,1]
	v_mov_b32_e32 v1, v3
	v_cvt_pk_fp8_f32 v1, v80, v81
	v_add_co_u32_e32 v56, vcc, s0, v76
	v_cvt_pk_fp8_f32 v1, v92, v93 op_sel:[0,0,1]
	s_nop 0
	v_addc_co_u32_e32 v57, vcc, 0, v77, vcc
	global_store_dwordx4 v[56:57], v[96:99], off
	v_add_co_u32_e32 v56, vcc, 0x15000000, v74
	s_nop 1
	v_addc_co_u32_e32 v57, vcc, 0, v75, vcc
	global_store_dword v[56:57], v1, off offset:128
	v_mov_b32_e32 v1, v3
	v_cvt_pk_fp8_f32 v1, v58, v59
	v_cvt_pk_fp8_f32 v1, v78, v79 op_sel:[0,0,1]
	global_store_dword v[56:57], v1, off offset:160
	s_cbranch_scc1 .LBB0_596

.LBB0_1757:
	v_lshl_add_u64 v[24:25], v[20:21], 0, s[72:73]
	global_load_dwordx4 v[32:35], v[24:25], off offset:-2032
	global_load_dwordx4 v[40:43], v[24:25], off offset:-2048
	s_waitcnt vmcnt(1)
	v_lshlrev_b32_e32 v26, 16, v34
	s_waitcnt vmcnt(0)
	v_lshlrev_b32_e32 v44, 16, v40
	v_and_b32_e32 v45, 0xffff0000, v40
	v_lshlrev_b32_e32 v40, 16, v41
	v_and_b32_e32 v41, 0xffff0000, v41
	v_lshlrev_b32_e32 v47, 16, v43
	v_lshlrev_b32_e32 v46, 16, v42
	v_and_b32_e32 v43, 0xffff0000, v43
	v_and_b32_e32 v42, 0xffff0000, v42
	v_mul_f32_e32 v2, v44, v44
	v_mul_f32_e32 v22, v40, v40
	v_lshlrev_b32_e32 v48, 16, v32
	v_and_b32_e32 v49, 0xffff0000, v32
	v_lshlrev_b32_e32 v50, 16, v33
	v_and_b32_e32 v51, 0xffff0000, v33
	v_pk_mul_f32 v[32:33], v[42:43], v[42:43]
	v_pk_fma_f32 v[56:57], v[44:45], v[44:45], v[2:3] op_sel_hi:[1,1,0]
	v_pk_fma_f32 v[22:23], v[40:41], v[40:41], v[22:23] op_sel_hi:[1,1,0]
	v_and_b32_e32 v31, 0xffff0000, v34
	v_mul_f32_e32 v34, v48, v48
	v_mul_f32_e32 v52, v50, v50
	v_mov_b32_e32 v54, v26
	v_pk_fma_f32 v[32:33], v[46:47], v[46:47], v[32:33]
	v_mov_b32_e32 v27, v57
	v_mov_b32_e32 v55, v23
	v_lshlrev_b32_e32 v28, 16, v35
	v_and_b32_e32 v29, 0xffff0000, v35
	v_pk_fma_f32 v[34:35], v[48:49], v[48:49], v[34:35] op_sel_hi:[1,1,0]
	v_pk_fma_f32 v[52:53], v[50:51], v[50:51], v[52:53] op_sel_hi:[1,1,0]
	v_pk_add_f32 v[32:33], v[32:33], v[32:33] op_sel_hi:[0,1]
	v_pk_add_f32 v[22:23], v[56:57], v[22:23]
	v_pk_mul_f32 v[54:55], v[26:27], v[54:55]
	v_mul_f32_e32 v34, v28, v28
	v_mul_f32_e32 v52, v29, v29
	v_mul_f32_e32 v32, v31, v31
	v_mov_b32_e32 v55, v23
	v_pk_add_f32 v[34:35], v[34:35], v[52:53]
	v_pk_add_f32 v[22:23], v[54:55], v[32:33]
	v_mov_b32_e32 v52, v46
	v_pk_add_f32 v[22:23], v[22:23], v[34:35]
	v_mov_b32_e32 v53, v42
	v_add_f32_e32 v2, v22, v23
	v_mov_b32_e32 v42, v47
	v_mov_b32_e32 v32, v3
	v_mov_b32_e32 v33, v3
	v_mov_b32_e32 v34, v3
	s_waitcnt lgkmcnt(0)
	s_nop 1
	v_add_f32_dpp v2, v2, v2 quad_perm:[1,0,3,2] row_mask:0xf bank_mask:0xf
	v_mov_b32_e32 v35, v3
	s_waitcnt lgkmcnt(0)
	s_nop 1
	v_add_f32_dpp v2, v2, v2 quad_perm:[2,3,0,1] row_mask:0xf bank_mask:0xf
	s_waitcnt lgkmcnt(0)
	s_nop 1
	v_add_f32_dpp v2, v2, v2 row_half_mirror row_mask:0xf bank_mask:0xf
	s_waitcnt lgkmcnt(0)
	s_nop 1
	v_add_f32_dpp v2, v2, v2 row_ror:8 row_mask:0xf bank_mask:0xf
	s_waitcnt lgkmcnt(0)
	v_mov_b32_e32 v22, v2
	s_nop 1
	v_permlane16_swap_b32_e32 v22, v2
	v_add_f32_e32 v2, v2, v22
	v_lshl_add_u64 v[22:23], v[16:17], 0, s[72:73]
	s_waitcnt lgkmcnt(0)
	v_mov_b32_e32 v27, v2
	s_nop 1
	v_permlane32_swap_b32_e32 v27, v2
	v_add_f32_e32 v2, v2, v27
	v_fmamk_f32 v2, v2, 0x3a800000, v220
	v_mul_f32_e32 v27, 0x4f800000, v2
	v_cmp_gt_f32_e32 vcc, s93, v2
	s_nop 1
	v_cndmask_b32_e32 v2, v2, v27, vcc
	v_sqrt_f32_e32 v27, v2
	s_nop 0
	v_add_u32_e32 v46, -1, v27
	v_add_u32_e32 v47, 1, v27
	v_fma_f32 v54, -v46, v27, v2
	v_fma_f32 v55, -v47, v27, v2
	v_cmp_ge_f32_e64 s[0:1], 0, v54
	s_nop 1
	v_cndmask_b32_e64 v27, v27, v46, s[0:1]
	v_cmp_lt_f32_e64 s[0:1], 0, v55
	s_nop 1
	v_cndmask_b32_e64 v27, v27, v47, s[0:1]
	v_mul_f32_e32 v46, 0x37800000, v27
	v_cndmask_b32_e32 v27, v27, v46, vcc
	v_cmp_class_f32_e32 vcc, v2, v221
	s_nop 1
	v_cndmask_b32_e32 v2, v27, v2, vcc
	v_div_scale_f32 v46, s[0:1], v2, v2, 1.0
	v_rcp_f32_e32 v47, v46
	v_mov_b32_e32 v27, v31
	v_div_scale_f32 v31, vcc, 1.0, v2, 1.0
	v_fma_f32 v54, -v46, v47, 1.0
	v_fmac_f32_e32 v47, v54, v47
	v_mul_f32_e32 v54, v31, v47
	v_fma_f32 v55, -v46, v54, v31
	v_fmac_f32_e32 v54, v55, v47
	v_fma_f32 v31, -v46, v54, v31
	v_div_fmas_f32 v31, v31, v47, v54
	v_div_fixup_f32 v2, v31, v2, 1.0
	v_pk_mul_f32 v[44:45], v[2:3], v[44:45] op_sel_hi:[0,1]
	v_pk_mul_f32 v[52:53], v[2:3], v[52:53] op_sel_hi:[0,1]
	v_pk_mul_f32 v[48:49], v[2:3], v[48:49] op_sel_hi:[0,1]
	v_pk_mul_f32 v[26:27], v[26:27], v[2:3] op_sel_hi:[1,0]
	v_pk_mul_f32 v[44:45], v[36:37], v[44:45]
	v_pk_mul_f32 v[52:53], v[12:13], v[52:53]
	v_pk_mul_f32 v[48:49], v[8:9], v[48:49]
	v_pk_mul_f32 v[26:27], v[4:5], v[26:27]
	v_cvt_pk_fp8_f32 v32, v44, v45
	v_cvt_pk_fp8_f32 v33, v52, v53
	v_cvt_pk_fp8_f32 v34, v48, v49
	v_cvt_pk_fp8_f32 v35, v26, v27
	v_pk_mul_f32 v[40:41], v[2:3], v[40:41] op_sel_hi:[0,1]
	v_pk_mul_f32 v[42:43], v[2:3], v[42:43] op_sel_hi:[0,1]
	v_pk_mul_f32 v[50:51], v[2:3], v[50:51] op_sel_hi:[0,1]
	v_pk_mul_f32 v[28:29], v[28:29], v[2:3] op_sel_hi:[1,0]
	v_pk_mul_f32 v[40:41], v[38:39], v[40:41]
	v_pk_mul_f32 v[42:43], v[14:15], v[42:43]
	v_pk_mul_f32 v[50:51], v[10:11], v[50:51]
	v_pk_mul_f32 v[28:29], v[6:7], v[28:29]
	v_cvt_pk_fp8_f32 v32, v40, v41 op_sel:[0,0,1]
	v_cvt_pk_fp8_f32 v33, v42, v43 op_sel:[0,0,1]
	v_cvt_pk_fp8_f32 v34, v50, v51 op_sel:[0,0,1]
	v_cvt_pk_fp8_f32 v35, v28, v29 op_sel:[0,0,1]
	v_add_co_u32_e32 v46, vcc, 0x48000000, v22
	v_add_u32_e32 v26, s2, v30
	s_nop 0
	v_addc_co_u32_e32 v47, vcc, 0, v23, vcc
	global_store_dwordx4 v[46:47], v[32:35], off
	s_and_saveexec_b64 s[0:1], s[6:7]
	s_cbranch_execz .LBB0_1759
	v_add_u32_e32 v2, 0x22680, v26
	ds_read_b32 v2, v2
	s_waitcnt lgkmcnt(0)
	v_bfe_u32 v27, v2, 16, 16
	v_and_b32_e32 v2, 0xffff, v2
	v_lshl_add_u32 v2, v27, 14, v2
	v_lshl_add_u64 v[28:29], v[2:3], 2, s[4:5]
	v_mov_b32_e32 v2, s8
	global_store_dword v[28:29], v2, off
.LBB0_1759:
	s_or_b64 exec, exec, s[0:1]
	global_load_dwordx4 v[32:35], v[24:25], off offset:16
	global_load_dwordx4 v[40:43], v[24:25], off
	s_waitcnt vmcnt(1)
	v_lshlrev_b32_e32 v48, 16, v32
	s_waitcnt vmcnt(0)
	v_lshlrev_b32_e32 v44, 16, v40
	v_and_b32_e32 v45, 0xffff0000, v40
	v_lshlrev_b32_e32 v40, 16, v41
	v_and_b32_e32 v41, 0xffff0000, v41
	v_lshlrev_b32_e32 v47, 16, v43
	v_lshlrev_b32_e32 v46, 16, v42
	v_and_b32_e32 v43, 0xffff0000, v43
	v_and_b32_e32 v42, 0xffff0000, v42
	v_and_b32_e32 v49, 0xffff0000, v32
	v_mul_f32_e32 v2, v44, v44
	v_mul_f32_e32 v32, v40, v40
	v_lshlrev_b32_e32 v24, 16, v34
	v_and_b32_e32 v27, 0xffff0000, v34
	v_lshlrev_b32_e32 v28, 16, v35
	v_and_b32_e32 v29, 0xffff0000, v35
	v_lshlrev_b32_e32 v50, 16, v33
	v_and_b32_e32 v51, 0xffff0000, v33
	v_pk_mul_f32 v[34:35], v[42:43], v[42:43]
	v_pk_fma_f32 v[58:59], v[44:45], v[44:45], v[2:3] op_sel_hi:[1,1,0]
	v_pk_fma_f32 v[32:33], v[40:41], v[40:41], v[32:33] op_sel_hi:[1,1,0]
	v_mul_f32_e32 v52, v48, v48
	v_mul_f32_e32 v54, v50, v50
	v_mov_b32_e32 v56, v24
	v_pk_fma_f32 v[34:35], v[46:47], v[46:47], v[34:35]
	v_mov_b32_e32 v25, v59
	v_mov_b32_e32 v57, v33
	v_pk_fma_f32 v[52:53], v[48:49], v[48:49], v[52:53] op_sel_hi:[1,1,0]
	v_pk_fma_f32 v[54:55], v[50:51], v[50:51], v[54:55] op_sel_hi:[1,1,0]
	v_pk_add_f32 v[34:35], v[34:35], v[34:35] op_sel_hi:[0,1]
	v_pk_add_f32 v[32:33], v[58:59], v[32:33]
	v_pk_mul_f32 v[56:57], v[24:25], v[56:57]
	v_mul_f32_e32 v52, v28, v28
	v_mul_f32_e32 v54, v29, v29
	v_mul_f32_e32 v34, v27, v27
	v_mov_b32_e32 v57, v33
	v_pk_add_f32 v[52:53], v[52:53], v[54:55]
	v_pk_add_f32 v[32:33], v[56:57], v[34:35]
	v_mov_b32_e32 v34, v3
	v_pk_add_f32 v[32:33], v[32:33], v[52:53]
	v_mov_b32_e32 v52, v46
	v_add_f32_e32 v2, v32, v33
	v_mov_b32_e32 v53, v42
	v_mov_b32_e32 v42, v47
	v_mov_b32_e32 v32, v3
	v_mov_b32_e32 v33, v3
	s_waitcnt lgkmcnt(0)
	s_nop 1
	v_add_f32_dpp v2, v2, v2 quad_perm:[1,0,3,2] row_mask:0xf bank_mask:0xf
	v_mov_b32_e32 v35, v3
	s_waitcnt lgkmcnt(0)
	s_nop 1
	v_add_f32_dpp v2, v2, v2 quad_perm:[2,3,0,1] row_mask:0xf bank_mask:0xf
	s_waitcnt lgkmcnt(0)
	s_nop 1
	v_add_f32_dpp v2, v2, v2 row_half_mirror row_mask:0xf bank_mask:0xf
	s_waitcnt lgkmcnt(0)
	s_nop 1
	v_add_f32_dpp v2, v2, v2 row_ror:8 row_mask:0xf bank_mask:0xf
	s_waitcnt lgkmcnt(0)
	v_mov_b32_e32 v25, v2
	s_nop 1
	v_permlane16_swap_b32_e32 v25, v2
	v_add_f32_e32 v2, v2, v25
	s_waitcnt lgkmcnt(0)
	v_mov_b32_e32 v25, v2
	s_nop 1
	v_permlane32_swap_b32_e32 v25, v2
	v_add_f32_e32 v2, v2, v25
	v_fmamk_f32 v2, v2, 0x3a800000, v220
	v_mul_f32_e32 v25, 0x4f800000, v2
	v_cmp_gt_f32_e32 vcc, s93, v2
	s_nop 1
	v_cndmask_b32_e32 v2, v2, v25, vcc
	v_sqrt_f32_e32 v25, v2
	s_nop 0
	v_add_u32_e32 v31, -1, v25
	v_add_u32_e32 v46, 1, v25
	v_fma_f32 v47, -v31, v25, v2
	v_fma_f32 v54, -v46, v25, v2
	v_cmp_ge_f32_e64 s[0:1], 0, v47
	s_nop 1
	v_cndmask_b32_e64 v25, v25, v31, s[0:1]
	v_cmp_lt_f32_e64 s[0:1], 0, v54
	s_nop 1
	v_cndmask_b32_e64 v25, v25, v46, s[0:1]
	v_mul_f32_e32 v31, 0x37800000, v25
	v_cndmask_b32_e32 v25, v25, v31, vcc
	v_cmp_class_f32_e32 vcc, v2, v221
	s_nop 1
	v_cndmask_b32_e32 v2, v25, v2, vcc
	v_div_scale_f32 v31, s[0:1], v2, v2, 1.0
	v_rcp_f32_e32 v46, v31
	v_mov_b32_e32 v25, v27
	v_div_scale_f32 v27, vcc, 1.0, v2, 1.0
	v_fma_f32 v47, -v31, v46, 1.0
	v_fmac_f32_e32 v46, v47, v46
	v_mul_f32_e32 v47, v27, v46
	v_fma_f32 v54, -v31, v47, v27
	v_fmac_f32_e32 v47, v54, v46
	v_fma_f32 v27, -v31, v47, v27
	v_div_fmas_f32 v27, v27, v46, v47
	v_div_fixup_f32 v2, v27, v2, 1.0
	v_pk_mul_f32 v[44:45], v[2:3], v[44:45] op_sel_hi:[0,1]
	v_pk_mul_f32 v[46:47], v[2:3], v[52:53] op_sel_hi:[0,1]
	v_pk_mul_f32 v[48:49], v[2:3], v[48:49] op_sel_hi:[0,1]
	v_pk_mul_f32 v[24:25], v[24:25], v[2:3] op_sel_hi:[1,0]
	v_pk_mul_f32 v[44:45], v[36:37], v[44:45]
	v_pk_mul_f32 v[46:47], v[12:13], v[46:47]
	v_pk_mul_f32 v[48:49], v[8:9], v[48:49]
	v_pk_mul_f32 v[24:25], v[4:5], v[24:25]
	v_cvt_pk_fp8_f32 v32, v44, v45
	v_cvt_pk_fp8_f32 v33, v46, v47
	v_cvt_pk_fp8_f32 v34, v48, v49
	v_cvt_pk_fp8_f32 v35, v24, v25
	v_pk_mul_f32 v[40:41], v[2:3], v[40:41] op_sel_hi:[0,1]
	v_pk_mul_f32 v[42:43], v[2:3], v[42:43] op_sel_hi:[0,1]
	v_pk_mul_f32 v[50:51], v[2:3], v[50:51] op_sel_hi:[0,1]
	v_pk_mul_f32 v[28:29], v[28:29], v[2:3] op_sel_hi:[1,0]
	v_pk_mul_f32 v[40:41], v[38:39], v[40:41]
	v_pk_mul_f32 v[42:43], v[14:15], v[42:43]
	v_pk_mul_f32 v[50:51], v[10:11], v[50:51]
	v_pk_mul_f32 v[28:29], v[6:7], v[28:29]
	v_cvt_pk_fp8_f32 v32, v40, v41 op_sel:[0,0,1]
	v_cvt_pk_fp8_f32 v33, v42, v43 op_sel:[0,0,1]
	v_cvt_pk_fp8_f32 v34, v50, v51 op_sel:[0,0,1]
	v_cvt_pk_fp8_f32 v35, v28, v29 op_sel:[0,0,1]
	v_add_co_u32_e32 v22, vcc, 0x48000000, v22
	s_nop 1
	v_addc_co_u32_e32 v23, vcc, 0, v23, vcc
	global_store_dwordx4 v[22:23], v[32:35], off offset:1024
	s_and_saveexec_b64 s[0:1], s[6:7]
	s_cbranch_execz .LBB0_1756
	v_add_u32_e32 v2, 0x22690, v26
	ds_read_b32 v2, v2
	s_add_i32 s3, s8, 1
	s_waitcnt lgkmcnt(0)
	v_bfe_u32 v22, v2, 16, 16
	v_and_b32_e32 v2, 0xffff, v2
	v_lshl_add_u32 v2, v22, 14, v2
	v_lshl_add_u64 v[22:23], v[2:3], 2, s[4:5]
	v_mov_b32_e32 v2, s3
	global_store_dword v[22:23], v2, off
	s_branch .LBB0_1756

.LBB0_2047:
	v_cndmask_b32_e64 v2, 0, 1, s[18:19]
	v_cmp_ne_u32_e64 s[6:7], 1, v2
	s_andn2_b64 vcc, exec, s[18:19]
	s_cbranch_vccnz .LBB0_2049
	v_pk_mul_f32 v[70:71], v[36:37], v[36:37]
	v_pk_mul_f32 v[72:73], v[38:39], v[38:39]
	v_add_f32_e32 v2, v70, v71
	v_add_f32_e32 v2, v2, v72
	v_pk_mul_f32 v[74:75], v[40:41], v[40:41]
	v_add_f32_e32 v2, v73, v2
	v_add_f32_e32 v2, v74, v2
	v_pk_mul_f32 v[76:77], v[42:43], v[42:43]
	v_add_f32_e32 v2, v75, v2
	v_add_f32_e32 v2, v76, v2
	v_pk_mul_f32 v[78:79], v[28:29], v[28:29]
	v_add_f32_e32 v2, v77, v2
	v_add_f32_e32 v2, v78, v2
	v_pk_mul_f32 v[80:81], v[30:31], v[30:31]
	v_add_f32_e32 v2, v79, v2
	v_add_f32_e32 v2, v80, v2
	v_pk_mul_f32 v[82:83], v[32:33], v[32:33]
	v_add_f32_e32 v2, v81, v2
	v_add_f32_e32 v2, v82, v2
	v_pk_mul_f32 v[84:85], v[34:35], v[34:35]
	v_add_f32_e32 v2, v83, v2
	v_add_f32_e32 v2, v84, v2
	v_add_f32_e32 v2, v85, v2
	s_waitcnt lgkmcnt(0)
	s_nop 1
	v_add_f32_dpp v2, v2, v2 quad_perm:[1,0,3,2] row_mask:0xf bank_mask:0xf
	s_waitcnt lgkmcnt(0)
	s_nop 1
	v_add_f32_dpp v2, v2, v2 quad_perm:[2,3,0,1] row_mask:0xf bank_mask:0xf
	s_waitcnt lgkmcnt(0)
	s_nop 1
	v_add_f32_dpp v2, v2, v2 row_half_mirror row_mask:0xf bank_mask:0xf
	s_waitcnt lgkmcnt(0)
	s_nop 1
	v_add_f32_dpp v2, v2, v2 row_ror:8 row_mask:0xf bank_mask:0xf
	s_waitcnt lgkmcnt(0)
	v_mov_b32_e32 v70, v2
	s_nop 1
	v_permlane16_swap_b32_e32 v70, v2
	v_add_f32_e32 v2, v2, v70
	s_waitcnt lgkmcnt(0)
	v_mov_b32_e32 v70, v2
	s_nop 1
	v_permlane32_swap_b32_e32 v70, v2
	v_add_f32_e32 v2, v2, v70
	v_fmamk_f32 v2, v2, 0x3a800000, v220
	v_cmp_gt_f32_e32 vcc, s93, v2
	v_mul_f32_e32 v70, 0x4f800000, v2
	s_nop 0
	v_cndmask_b32_e32 v2, v2, v70, vcc
	v_sqrt_f32_e32 v70, v2
	s_nop 0
	v_add_u32_e32 v71, -1, v70
	v_fma_f32 v72, -v71, v70, v2
	v_cmp_ge_f32_e64 s[0:1], 0, v72
	v_add_u32_e32 v72, 1, v70
	s_nop 0
	v_cndmask_b32_e64 v71, v70, v71, s[0:1]
	v_fma_f32 v70, -v72, v70, v2
	v_cmp_lt_f32_e64 s[0:1], 0, v70
	s_nop 1
	v_cndmask_b32_e64 v70, v71, v72, s[0:1]
	v_mul_f32_e32 v71, 0x37800000, v70
	v_cndmask_b32_e32 v70, v70, v71, vcc
	v_cmp_class_f32_e32 vcc, v2, v221
	s_nop 1
	v_cndmask_b32_e32 v2, v70, v2, vcc
	v_div_scale_f32 v70, s[0:1], v2, v2, 1.0
	v_rcp_f32_e32 v71, v70
	s_lshl_b64 s[0:1], s[22:23], 10
	v_fma_f32 v72, -v70, v71, 1.0
	v_fmac_f32_e32 v71, v72, v71
	v_div_scale_f32 v72, vcc, 1.0, v2, 1.0
	v_mul_f32_e32 v73, v72, v71
	v_fma_f32 v74, -v70, v73, v72
	v_fmac_f32_e32 v73, v74, v71
	v_fma_f32 v70, -v70, v73, v72
	v_div_fmas_f32 v70, v70, v71, v73
	v_div_fixup_f32 v2, v70, v2, 1.0
	global_load_dwordx4 v[70:73], v[16:17], off offset:16
	global_load_dwordx4 v[74:77], v[16:17], off
	v_mul_f32_e32 v36, v36, v2
	v_mul_f32_e32 v28, v28, v2
	s_waitcnt vmcnt(0)
	v_mul_f32_e32 v74, v74, v36
	v_mul_f32_e32 v36, v37, v2
	v_mul_f32_e32 v75, v75, v36
	v_mul_f32_e32 v36, v38, v2
	v_mul_f32_e32 v76, v76, v36
	v_mul_f32_e32 v36, v39, v2
	v_mul_f32_e32 v77, v77, v36
	v_mul_f32_e32 v36, v40, v2
	v_mul_f32_e32 v70, v70, v36
	v_mul_f32_e32 v36, v41, v2
	v_mul_f32_e32 v71, v71, v36
	v_mul_f32_e32 v36, v42, v2
	v_mul_f32_e32 v72, v72, v36
	v_mul_f32_e32 v36, v43, v2
	v_mul_f32_e32 v73, v73, v36
	global_load_dwordx4 v[36:39], v[16:17], off offset:2064
	global_load_dwordx4 v[40:43], v[16:17], off offset:2048
	s_waitcnt vmcnt(0)
	v_mul_f32_e32 v40, v40, v28
	v_mul_f32_e32 v28, v29, v2
	v_mul_f32_e32 v41, v41, v28
	v_mul_f32_e32 v28, v30, v2
	v_mul_f32_e32 v42, v42, v28
	v_mul_f32_e32 v28, v31, v2
	v_mul_f32_e32 v43, v43, v28
	v_mul_f32_e32 v28, v32, v2
	v_mul_f32_e32 v32, v36, v28
	v_mul_f32_e32 v28, v33, v2
	v_mul_f32_e32 v33, v37, v28
	v_mul_f32_e32 v28, v34, v2
	v_mul_f32_e32 v34, v38, v28
	v_mov_b32_e32 v28, v3
	v_mov_b32_e32 v29, v3
	v_cvt_pk_fp8_f32 v28, v74, v75
	v_cvt_pk_fp8_f32 v29, v70, v71
	v_lshl_add_u64 v[30:31], v[50:51], 0, s[0:1]
	v_mul_f32_e32 v2, v35, v2
	v_cvt_pk_fp8_f32 v28, v76, v77 op_sel:[0,0,1]
	v_cvt_pk_fp8_f32 v29, v72, v73 op_sel:[0,0,1]
	v_mul_f32_e32 v2, v39, v2
	global_store_dwordx2 v[30:31], v[28:29], off
	v_mov_b32_e32 v28, v3
	v_mov_b32_e32 v29, v3
	v_cvt_pk_fp8_f32 v28, v40, v41
	v_cvt_pk_fp8_f32 v29, v32, v33
	v_cvt_pk_fp8_f32 v28, v42, v43 op_sel:[0,0,1]
	v_cvt_pk_fp8_f32 v29, v34, v2 op_sel:[0,0,1]
	global_store_dwordx2 v[30:31], v[28:29], off offset:512

.LBB0_2053:
	s_and_b64 vcc, exec, s[6:7]
	s_cbranch_vccnz .LBB0_2043
	v_pk_mul_f32 v[32:33], v[28:29], v[28:29]
	v_pk_mul_f32 v[34:35], v[30:31], v[30:31]
	v_add_f32_e32 v2, v32, v33
	v_add_f32_e32 v2, v2, v34
	v_pk_mul_f32 v[36:37], v[24:25], v[24:25]
	v_add_f32_e32 v2, v35, v2
	v_add_f32_e32 v2, v36, v2
	v_pk_mul_f32 v[38:39], v[26:27], v[26:27]
	v_add_f32_e32 v2, v37, v2
	v_add_f32_e32 v2, v38, v2
	v_pk_mul_f32 v[40:41], v[12:13], v[12:13]
	v_add_f32_e32 v2, v39, v2
	v_add_f32_e32 v2, v40, v2
	v_pk_mul_f32 v[42:43], v[14:15], v[14:15]
	v_add_f32_e32 v2, v41, v2
	v_add_f32_e32 v2, v42, v2
	v_pk_mul_f32 v[52:53], v[20:21], v[20:21]
	v_add_f32_e32 v2, v43, v2
	v_add_f32_e32 v2, v52, v2
	v_pk_mul_f32 v[54:55], v[22:23], v[22:23]
	v_add_f32_e32 v2, v53, v2
	v_add_f32_e32 v2, v54, v2
	v_add_f32_e32 v2, v55, v2
	s_ashr_i32 s21, s20, 31
	s_waitcnt lgkmcnt(0)
	s_nop 1
	v_add_f32_dpp v2, v2, v2 quad_perm:[1,0,3,2] row_mask:0xf bank_mask:0xf
	s_waitcnt lgkmcnt(0)
	s_nop 1
	v_add_f32_dpp v2, v2, v2 quad_perm:[2,3,0,1] row_mask:0xf bank_mask:0xf
	s_waitcnt lgkmcnt(0)
	s_nop 1
	v_add_f32_dpp v2, v2, v2 row_half_mirror row_mask:0xf bank_mask:0xf
	s_waitcnt lgkmcnt(0)
	s_nop 1
	v_add_f32_dpp v2, v2, v2 row_ror:8 row_mask:0xf bank_mask:0xf
	s_waitcnt lgkmcnt(0)
	v_mov_b32_e32 v32, v2
	s_nop 1
	v_permlane16_swap_b32_e32 v32, v2
	v_add_f32_e32 v2, v2, v32
	s_waitcnt lgkmcnt(0)
	v_mov_b32_e32 v32, v2
	s_nop 1
	v_permlane32_swap_b32_e32 v32, v2
	v_add_f32_e32 v2, v2, v32
	v_fmamk_f32 v2, v2, 0x3a800000, v220
	v_cmp_gt_f32_e32 vcc, s93, v2
	v_mul_f32_e32 v32, 0x4f800000, v2
	s_nop 0
	v_cndmask_b32_e32 v2, v2, v32, vcc
	v_sqrt_f32_e32 v32, v2
	s_nop 0
	v_add_u32_e32 v33, -1, v32
	v_fma_f32 v34, -v33, v32, v2
	v_cmp_ge_f32_e64 s[0:1], 0, v34
	v_add_u32_e32 v34, 1, v32
	s_nop 0
	v_cndmask_b32_e64 v33, v32, v33, s[0:1]
	v_fma_f32 v32, -v34, v32, v2
	v_cmp_lt_f32_e64 s[0:1], 0, v32
	s_nop 1
	v_cndmask_b32_e64 v32, v33, v34, s[0:1]
	v_mul_f32_e32 v33, 0x37800000, v32
	v_cndmask_b32_e32 v32, v32, v33, vcc
	v_cmp_class_f32_e32 vcc, v2, v221
	s_nop 1
	v_cndmask_b32_e32 v2, v32, v2, vcc
	v_div_scale_f32 v32, s[0:1], v2, v2, 1.0
	v_rcp_f32_e32 v33, v32
	s_lshl_b64 s[0:1], s[20:21], 10
	v_fma_f32 v34, -v32, v33, 1.0
	v_fmac_f32_e32 v33, v34, v33
	v_div_scale_f32 v34, vcc, 1.0, v2, 1.0
	v_mul_f32_e32 v35, v34, v33
	v_fma_f32 v36, -v32, v35, v34
	v_fmac_f32_e32 v35, v36, v33
	v_fma_f32 v32, -v32, v35, v34
	v_div_fmas_f32 v32, v32, v33, v35
	v_div_fixup_f32 v2, v32, v2, 1.0
	global_load_dwordx4 v[32:35], v[16:17], off offset:16
	global_load_dwordx4 v[36:39], v[16:17], off
	v_mul_f32_e32 v28, v28, v2
	v_mul_f32_e32 v24, v24, v2
	v_mul_f32_e32 v12, v12, v2
	s_waitcnt vmcnt(1)
	v_mul_f32_e32 v32, v32, v24
	s_waitcnt vmcnt(0)
	v_mul_f32_e32 v36, v36, v28
	v_mul_f32_e32 v28, v29, v2
	v_mul_f32_e32 v24, v25, v2
	v_mul_f32_e32 v37, v37, v28
	v_mul_f32_e32 v28, v30, v2
	v_mul_f32_e32 v33, v33, v24
	v_mul_f32_e32 v24, v26, v2
	v_mul_f32_e32 v38, v38, v28
	v_mul_f32_e32 v28, v31, v2
	v_mul_f32_e32 v34, v34, v24
	v_mul_f32_e32 v24, v27, v2
	v_mul_f32_e32 v39, v39, v28
	v_mul_f32_e32 v35, v35, v24
	global_load_dwordx4 v[24:27], v[16:17], off offset:2064
	global_load_dwordx4 v[28:31], v[16:17], off offset:2048
	s_waitcnt vmcnt(0)
	v_mul_f32_e32 v28, v28, v12
	v_mul_f32_e32 v12, v13, v2
	v_mul_f32_e32 v29, v29, v12
	v_mul_f32_e32 v12, v14, v2
	v_mul_f32_e32 v30, v30, v12
	v_mul_f32_e32 v12, v15, v2
	v_mul_f32_e32 v31, v31, v12
	v_mul_f32_e32 v12, v20, v2
	v_mul_f32_e32 v20, v24, v12
	v_mul_f32_e32 v12, v21, v2
	v_mul_f32_e32 v21, v25, v12
	v_mul_f32_e32 v12, v22, v2
	v_mul_f32_e32 v22, v26, v12
	v_mov_b32_e32 v12, v3
	v_mov_b32_e32 v13, v3
	v_cvt_pk_fp8_f32 v12, v36, v37
	v_cvt_pk_fp8_f32 v13, v32, v33
	v_lshl_add_u64 v[14:15], v[50:51], 0, s[0:1]
	v_mul_f32_e32 v2, v23, v2
	v_cvt_pk_fp8_f32 v12, v38, v39 op_sel:[0,0,1]
	v_cvt_pk_fp8_f32 v13, v34, v35 op_sel:[0,0,1]
	v_mul_f32_e32 v2, v27, v2
	global_store_dwordx2 v[14:15], v[12:13], off
	v_mov_b32_e32 v12, v3
	v_mov_b32_e32 v13, v3
	v_cvt_pk_fp8_f32 v12, v28, v29
	v_cvt_pk_fp8_f32 v13, v20, v21
	v_cvt_pk_fp8_f32 v12, v30, v31 op_sel:[0,0,1]
	v_cvt_pk_fp8_f32 v13, v22, v2 op_sel:[0,0,1]
	global_store_dwordx2 v[14:15], v[12:13], off offset:512
	s_branch .LBB0_2043
